# swa unit prologue: sinks load and tile-0 K/V loads issued with the Q/kmax batch (one round trip instead of three), counted waits
# speedup vs baseline: 1.0037x; 1.0037x over previous
; __device__ __forceinline__ float bflo(unsigned w) { return __uint_as_float(w << 16); }
;     ...
;         const int qi = 32 - u / 16, bk = u % 16, b = bk >> 1, hkv = bk & 1, hq = 2 * hkv + (wave >> 2);
;         const int q0 = qi == 0 ? 0 : 16 + 128 * (qi - 1);
;         const int ktlo = max(1, (q0 - 127) / 64), kthi = qi == 0 ? 0 : (q0 + 127) / 64;
;         const int ntile = 1 + (kthi >= ktlo ? kthi - ktlo + 1 : 0);
;         const int q0w = q0 + 32 * (wave & 3), qpos = q0w + l31;
;         const bool wave_on = (qi > 0) || ((wave & 3) == 0);
;         const size_t qrow = (size_t)b * LT + (qpos < LT ? qpos : LT - 1);
;         bf16x8 Qf[4]; bf16x8 qx; float lsum;
;         { u32x4 qraw[4]; float qn2 = 0.f;
; #pragma unroll
;           for (int s = 0; s < 4; ++s) qraw[s] = *(const u32x4*)(U + qrow * INW + C_QA + hq * 64 + s * 16 + hi * 8);
;           const float km2 = __uint_as_float(__hip_atomic_load((const unsigned*)(ws + WS_CTL) + CW_KMX + l * 256 + 128 + b * 2 + hkv, __ATOMIC_RELAXED, __HIP_MEMORY_SCOPE_AGENT));
; #pragma unroll
;           for (int s = 0; s < 4; ++s) { const unsigned qw[4] = {qraw[s].x, qraw[s].y, qraw[s].z, qraw[s].w}; u32x4 qs;
; #pragma unroll
;               for (int e = 0; e < 4; ++e) qn2 += bflo(qw[e]) * bflo(qw[e]) + bfhi(qw[e]) * bfhi(qw[e]);
;               qs.x = pkbf(bflo(qw[0]) * c2, bfhi(qw[0]) * c2); qs.y = pkbf(bflo(qw[1]) * c2, bfhi(qw[1]) * c2); qs.z = pkbf(bflo(qw[2]) * c2, bfhi(qw[2]) * c2); qs.w = pkbf(bflo(qw[3]) * c2, bfhi(qw[3]) * c2);
;               Qf[s] = __builtin_bit_cast(bf16x8, qs); }
;           qn2 += __shfl_xor(qn2, 32);
;           const float snk = p.in[I_SINKS][l * 4 + hq] * LOG2E;
;           const float mref = fmaxf(sqrtf(qn2 * km2) * 1.001f * c2 + btab[hq * 132 + 131], snk);
;           u32x4 qxw; qxw.x = hi ? 0u : (pkbf(-mref, 0.f) & 0xffffu); qxw.y = 0u; qxw.z = 0u; qxw.w = 0u; qx = __builtin_bit_cast(bf16x8, qxw);
;           const float mrb = bflo(pkbf(-mref, 0.f));
;           lsum = hi == 0 ? __builtin_amdgcn_exp2f(snk + mrb) : 0.0f; }
;     ...
;         const bf16_t* kbase = U + (size_t)b * LT * INW + C_KA + hkv * 64;
;         const bf16_t* vbase = VT + (size_t)bk * 64 * LTP;
;         const unsigned koff = (unsigned)(krow * INW + kch * 8), voff = (unsigned)(krow * LTP + kch * 8);
;         u32x4 kreg = *(const u32x4*)(kbase + koff), vreg = *(const u32x4*)(vbase + voff);
.LBB0_814:
	v_add_u32_e32 v2, v0, v2
	v_and_b32_e32 v2, -16, v2
	v_sub_u32_e32 v8, v0, v2
	v_and_b32_e32 v11, 1, v8
	v_lshlrev_b32_e32 v2, 1, v11
	s_waitcnt vmcnt(0)
	v_add_u32_e32 v76, s34, v2
	v_add_u32_e32 v2, 0xffffff81, v50
	v_ashrrev_i32_e32 v3, 31, v2
	v_lshrrev_b32_e32 v3, 26, v3
	v_add_u32_e32 v2, v2, v3
	v_ashrrev_i32_e32 v2, 6, v2
	v_max_i32_e32 v51, 1, v2
	v_add_u32_e32 v2, 0x7f, v50
	v_lshrrev_b32_e32 v2, 6, v2
	v_cndmask_b32_e64 v2, v2, 0, s[0:1]
	v_sub_co_u32_e32 v2, vcc, v2, v51
	v_lshrrev_b32_e32 v41, 1, v8
	v_readfirstlane_b32 s0, v2
	v_add_u32_e32 v120, s35, v50
	s_add_i32 s8, s0, 2
	v_add_u32_e32 v40, v120, v112
	s_movk_i32 s0, 0x200
	v_mul_lo_u32 v104, v41, s33
	v_cmp_gt_i32_e64 s[6:7], s0, v0
	v_ashrrev_i32_e32 v105, 31, v104
	v_min_i32_e32 v0, 0x100f, v40
	v_lshl_add_u64 v[2:3], v[0:1], 0, v[104:105]
	v_mov_b64_e32 v[4:5], s[16:17]
	v_mad_u64_u32 v[4:5], s[0:1], v2, s97, v[4:5]
	s_waitcnt vmcnt(0)
	v_lshlrev_b32_e32 v106, 6, v76
	v_mad_i32_i24 v5, v3, s97, v5
	v_ashrrev_i32_e32 v107, 31, v106
	v_lshl_add_u64 v[2:3], v[106:107], 1, v[4:5]
	v_mov_b32_e32 v103, v1
	v_lshl_add_u64 v[6:7], v[2:3], 0, v[102:103]
	global_load_dwordx4 v[2:5], v[6:7], off
	global_load_dwordx4 v[12:15], v[6:7], off offset:32
	global_load_dwordx4 v[42:45], v[6:7], off offset:64
	global_load_dwordx4 v[46:49], v[6:7], off offset:96
	v_and_b32_e32 v6, -2, v8
	v_ashrrev_i32_e32 v7, 31, v6
	v_lshlrev_b64 v[6:7], 2, v[6:7]
	s_and_b64 s[0:1], vcc, exec
	v_lshl_add_u64 v[6:7], s[26:27], 0, v[6:7]
	v_lshlrev_b32_e32 v0, 2, v11
	v_readfirstlane_b32 s1, v7
	v_readfirstlane_b32 s0, v6
	v_readlane_b32 s48, v253, 12
	v_readlane_b32 s58, v253, 22
	v_readlane_b32 s59, v253, 23
	s_cselect_b32 s37, 1, s8
	s_or_b64 s[28:29], s[6:7], s[24:25]
	global_load_dword v0, v0, s[0:1] sc1
	s_mov_b32 s0, 0xf800000
	s_cmp_lt_i32 s37, 1
	v_add_u32_e32 v144, s36, v76
	v_ashrrev_i32_e32 v145, 31, v144
	v_lshlrev_b64 v[144:145], 2, v[144:145]
	s_mov_b32 s30, 0x1616000
	v_mul_lo_u32 v148, v41, s30
	v_mul_hi_i32 v149, v104, s97
	v_lshl_add_u64 v[144:145], s[58:59], 0, v[144:145]
	global_load_dword v146, v[144:145], off
	v_lshl_add_u64 v[148:149], s[16:17], 0, v[148:149]
	v_lshlrev_b32_e32 v150, 7, v11
	v_mov_b32_e32 v151, 0
	v_lshl_add_u64 v[128:129], v[148:149], 0, v[150:151]
	s_mov_b32 s30, 0x41000
	v_mul_lo_u32 v148, v8, s30
	v_ashrrev_i32_e32 v149, 31, v148
	v_lshlrev_b64 v[148:149], 1, v[148:149]
	v_lshl_add_u64 v[130:131], s[18:19], 0, v[148:149]
	v_lshl_add_u64 v[148:149], v[98:99], 1, v[128:129]
	global_load_dwordx4 v[136:139], v[148:149], off offset:512
	v_lshl_add_u64 v[148:149], v[100:101], 1, v[130:131]
	global_load_dwordx4 v[140:143], v[148:149], off
	v_readlane_b32 s49, v253, 13
	v_readlane_b32 s50, v253, 14
	v_readlane_b32 s51, v253, 15
	v_readlane_b32 s52, v253, 16
	v_readlane_b32 s53, v253, 17
	v_readlane_b32 s54, v253, 18
	v_readlane_b32 s55, v253, 19
	v_readlane_b32 s56, v253, 20
	v_readlane_b32 s57, v253, 21
	v_readlane_b32 s60, v253, 24
	v_readlane_b32 s61, v253, 25
	v_readlane_b32 s62, v253, 26
	v_readlane_b32 s63, v253, 27
	s_waitcnt vmcnt(7)
	v_lshlrev_b32_e32 v20, 16, v2
	v_and_b32_e32 v21, 0xffff0000, v2
	v_lshlrev_b32_e32 v26, 16, v3
	s_waitcnt vmcnt(4)
; #define LAS __attribute__((address_space(3)))
; __device__ __forceinline__ float bflo(unsigned w) { return __uint_as_float(w << 16); }
; __device__ __forceinline__ float bfhi(unsigned w) { return __uint_as_float(w & 0xFFFF0000u); }
; __device__ __forceinline__ unsigned pkbf(float lo, float hi) { f32x2_t v = {lo, hi}; bf16x2_t b = __builtin_convertvector(v, bf16x2_t); return __builtin_bit_cast(unsigned, b); }
;     ...
;           for (int s = 0; s < 4; ++s) { const unsigned qw[4] = {qraw[s].x, qraw[s].y, qraw[s].z, qraw[s].w}; u32x4 qs;
; #pragma unroll
;               for (int e = 0; e < 4; ++e) qn2 += bflo(qw[e]) * bflo(qw[e]) + bfhi(qw[e]) * bfhi(qw[e]);
;               qs.x = pkbf(bflo(qw[0]) * c2, bfhi(qw[0]) * c2); qs.y = pkbf(bflo(qw[1]) * c2, bfhi(qw[1]) * c2); qs.z = pkbf(bflo(qw[2]) * c2, bfhi(qw[2]) * c2); qs.w = pkbf(bflo(qw[3]) * c2, bfhi(qw[3]) * c2);
;               Qf[s] = __builtin_bit_cast(bf16x8, qs); }
;           qn2 += __shfl_xor(qn2, 32);
;           const float snk = p.in[I_SINKS][l * 4 + hq] * LOG2E;
;           const float mref = fmaxf(sqrtf(qn2 * km2) * 1.001f * c2 + btab[hq * 132 + 131], snk);
;           u32x4 qxw; qxw.x = hi ? 0u : (pkbf(-mref, 0.f) & 0xffffu); qxw.y = 0u; qxw.z = 0u; qxw.w = 0u; qx = __builtin_bit_cast(bf16x8, qxw);
;           const float mrb = bflo(pkbf(-mref, 0.f));
;           lsum = hi == 0 ? __builtin_amdgcn_exp2f(snk + mrb) : 0.0f; }
;         f32x16 O[2];
; #pragma unroll
;         for (int d = 0; d < 2; ++d)
; #pragma unroll
;             for (int r = 0; r < 16; ++r) O[d][r] = 0.f;
;         const bf16_t* kbase = U + (size_t)b * LT * INW + C_KA + hkv * 64;
;         const bf16_t* vbase = VT + (size_t)bk * 64 * LTP;
;         const unsigned koff = (unsigned)(krow * INW + kch * 8), voff = (unsigned)(krow * LTP + kch * 8);
;         u32x4 kreg = *(const u32x4*)(kbase + koff), vreg = *(const u32x4*)(vbase + voff);
;         *(LAS u32x4*)(KV + krow * DF_PITCH + kch * 16) = kreg; *(LAS u32x4*)(KV + 2 * DF_KB + krow * DF_PITCH + kch * 16) = vreg;
;         __syncthreads();
	v_and_b32_e32 v7, 0xffff0000, v47
	v_and_b32_e32 v27, 0xffff0000, v3
	v_lshlrev_b32_e32 v30, 16, v14
	v_and_b32_e32 v31, 0xffff0000, v14
	v_lshlrev_b32_e32 v36, 16, v15
	v_and_b32_e32 v37, 0xffff0000, v15
	v_lshlrev_b32_e32 v10, 16, v46
	v_and_b32_e32 v15, 0xffff0000, v46
	v_mov_b32_e32 v14, v7
	v_and_b32_e32 v9, 0xffff0000, v49
	v_pk_mul_f32 v[52:53], v[20:21], v[20:21]
	v_pk_mul_f32 v[54:55], v[26:27], v[26:27]
	v_lshlrev_b32_e32 v32, 16, v4
	v_and_b32_e32 v33, 0xffff0000, v4
	v_lshlrev_b32_e32 v38, 16, v5
	v_and_b32_e32 v39, 0xffff0000, v5
	v_lshlrev_b32_e32 v18, 16, v12
	v_and_b32_e32 v19, 0xffff0000, v12
	v_lshlrev_b32_e32 v24, 16, v13
	v_and_b32_e32 v25, 0xffff0000, v13
	v_lshlrev_b32_e32 v4, 16, v47
	v_mov_b32_e32 v5, v10
	v_pk_mul_f32 v[2:3], v[14:15], v[14:15]
	v_and_b32_e32 v13, 0xffff0000, v48
	v_mov_b32_e32 v12, v9
	v_pk_mul_f32 v[56:57], v[32:33], v[32:33]
	v_pk_fma_f32 v[46:47], v[4:5], v[4:5], v[2:3]
	v_lshlrev_b32_e32 v6, 16, v48
	v_lshlrev_b32_e32 v2, 16, v49
	v_pk_mul_f32 v[48:49], v[12:13], v[12:13]
	v_add_f32_e32 v5, v54, v55
	v_add_f32_e32 v12, v52, v53
	v_pk_mul_f32 v[58:59], v[38:39], v[38:39]
	v_mov_b32_e32 v3, v6
	v_add_f32_e32 v5, v12, v5
	v_add_f32_e32 v12, v56, v57
	v_pk_mul_f32 v[60:61], v[18:19], v[18:19]
	v_pk_fma_f32 v[48:49], v[2:3], v[2:3], v[48:49]
	v_add_f32_e32 v3, v58, v59
	v_add_f32_e32 v5, v12, v5
	v_pk_mul_f32 v[62:63], v[24:25], v[24:25]
	v_add_f32_e32 v3, v3, v5
	v_add_f32_e32 v5, v60, v61
	v_pk_mul_f32 v[64:65], v[30:31], v[30:31]
	v_add_f32_e32 v3, v5, v3
	v_add_f32_e32 v5, v62, v63
	v_pk_mul_f32 v[70:71], v[36:37], v[36:37]
	v_lshlrev_b32_e32 v16, 16, v42
	v_and_b32_e32 v17, 0xffff0000, v42
	v_add_f32_e32 v3, v5, v3
	v_add_f32_e32 v5, v64, v65
	v_pk_mul_f32 v[72:73], v[16:17], v[16:17]
	v_lshlrev_b32_e32 v22, 16, v43
	v_and_b32_e32 v23, 0xffff0000, v43
	v_add_f32_e32 v3, v5, v3
	v_add_f32_e32 v5, v70, v71
	v_pk_mul_f32 v[42:43], v[22:23], v[22:23]
	v_lshlrev_b32_e32 v28, 16, v44
	v_and_b32_e32 v29, 0xffff0000, v44
	v_add_f32_e32 v3, v5, v3
	v_add_f32_e32 v5, v72, v73
	v_pk_mul_f32 v[74:75], v[28:29], v[28:29]
	v_lshlrev_b32_e32 v34, 16, v45
	v_and_b32_e32 v35, 0xffff0000, v45
	v_add_f32_e32 v3, v5, v3
	v_add_f32_e32 v5, v42, v43
	v_pk_mul_f32 v[44:45], v[34:35], v[34:35]
	v_add_f32_e32 v3, v5, v3
	v_add_f32_e32 v5, v74, v75
	v_add_f32_e32 v3, v5, v3
	v_add_f32_e32 v5, v44, v45
	v_add_f32_e32 v3, v5, v3
	v_and_b32_e32 v12, 64, v222
	v_add_f32_e32 v3, v47, v3
	v_xor_b32_e32 v5, 32, v222
	v_add_u32_e32 v12, 64, v12
	v_add_f32_e32 v3, v46, v3
	v_cmp_lt_i32_e32 vcc, v5, v12
	v_add_f32_e32 v3, v49, v3
	v_add_f32_e32 v3, v48, v3
	v_cndmask_b32_e32 v5, v222, v5, vcc
	v_lshlrev_b32_e32 v103, 2, v5
	ds_bpermute_b32 v5, v103, v3
	v_add_u32_e32 v42, s36, v76
	v_ashrrev_i32_e32 v43, 31, v42
	v_lshlrev_b64 v[42:43], 2, v[42:43]
	v_lshl_add_u64 v[42:43], s[58:59], 0, v[42:43]
	s_waitcnt lgkmcnt(0)
	v_add_f32_e32 v3, v3, v5
	s_nop 0
	s_waitcnt vmcnt(3)
	v_mul_f32_e32 v0, v3, v0
	v_cmp_gt_f32_e32 vcc, s0, v0
	v_mul_f32_e32 v3, 0x4f800000, v0
	v_mul_hi_i32 v43, v104, s97
	v_cndmask_b32_e32 v0, v0, v3, vcc
	v_sqrt_f32_e32 v3, v0
	s_nop 0
	v_add_u32_e32 v12, -1, v3
	v_fma_f32 v14, -v12, v3, v0
	v_cmp_ge_f32_e64 s[0:1], 0, v14
	v_add_u32_e32 v14, 1, v3
	s_nop 0
	v_cndmask_b32_e64 v12, v3, v12, s[0:1]
	v_fma_f32 v3, -v14, v3, v0
	v_cmp_lt_f32_e64 s[0:1], 0, v3
	s_nop 1
	v_cndmask_b32_e64 v3, v12, v14, s[0:1]
	v_mul_f32_e32 v12, 0x37800000, v3
	v_cndmask_b32_e32 v3, v3, v12, vcc
	v_cmp_class_f32_e32 vcc, v0, v250
	s_movk_i32 s0, 0x210
	s_nop 0
	v_cndmask_b32_e32 v0, v3, v0, vcc
	v_mul_lo_u32 v3, v76, s0
	v_add_u32_e32 v122, 0, v3
	ds_read_b32 v3, v122 offset:524
	v_mul_f32_e32 v0, 0x3f8020c5, v0
	s_mov_b32 s0, 0x1616000
	v_mul_lo_u32 v42, v41, s0
	v_lshl_add_u64 v[42:43], s[16:17], 0, v[42:43]
	s_waitcnt lgkmcnt(0)
	v_fmac_f32_e32 v3, 0x3e38aa3b, v0
	s_mov_b32 s0, 0x41000
	s_waitcnt vmcnt(2)
	v_mov_b32_e32 v5, v146
	v_mul_f32_e32 v0, 0xbfb8aa3b, v5
	v_min_f32_e64 v0, -v3, v0
	v_cvt_pk_bf16_f32 v3, v0, 0
	v_lshlrev_b32_e32 v0, 16, v3
	v_fmac_f32_e32 v0, 0x3fb8aa3b, v5
	v_exp_f32_e32 v0, v0
	s_nop 0
	v_cndmask_b32_e64 v121, 0, v0, s[4:5]
	v_lshlrev_b32_e32 v0, 7, v11
	v_lshl_add_u64 v[108:109], v[42:43], 0, v[0:1]
	v_mul_lo_u32 v42, v8, s0
	v_ashrrev_i32_e32 v43, 31, v42
	v_lshlrev_b64 v[42:43], 1, v[42:43]
	v_lshl_add_u64 v[110:111], s[18:19], 0, v[42:43]
	v_lshl_add_u64 v[42:43], v[98:99], 1, v[108:109]
	s_nop 0
	v_lshl_add_u64 v[42:43], v[100:101], 1, v[110:111]
	s_nop 0
	s_waitcnt vmcnt(1)
	ds_write_b128 v113, v[136:139] offset:8192
	s_waitcnt vmcnt(0)
	ds_write_b128 v113, v[140:143] offset:26624
	s_waitcnt lgkmcnt(0)
	s_barrier
	s_cbranch_scc1 .LBB0_819
	s_cmp_lg_u32 s37, 1
	s_mov_b32 s0, 0x2c000
	s_cselect_b64 s[30:31], -1, 0
	s_cmp_eq_u32 s37, 1
	v_mul_lo_u32 v52, v51, s0
	s_cbranch_scc1 .LBB0_817
	v_add_u32_e32 v0, v52, v98
	v_lshl_add_u64 v[42:43], v[0:1], 1, v[108:109]
	v_lshl_add_u32 v0, v51, 6, v100
	v_lshl_add_u64 v[44:45], v[0:1], 1, v[110:111]
	global_load_dwordx4 v[70:73], v[42:43], off offset:512
	global_load_dwordx4 v[74:77], v[44:45], off
